# W8 + final RMSNorm: gain vector loaded once before the row loop (was 8 serialised reloads per row) + prologue silu(cond) loop unrolled with all 16 loads in flight
# baseline (speedup 1.0000x reference)
.LBB0_94:
	s_movk_i32 s4, 0x2000
	v_cmp_gt_i32_e32 vcc, s4, v132
	s_barrier
	s_and_saveexec_b64 s[4:5], vcc
	s_cbranch_execz .LBB0_97
	v_readlane_b32 s12, v253, 1
	v_readlane_b32 s14, v253, 3
	v_readlane_b32 s15, v253, 4
	v_add_u32_e32 v2, 0xfffffe00, v132
	v_mov_b32_e32 v0, s14
	v_mov_b32_e32 v1, s15
	v_lshl_add_u32 v3, v132, 2, s48
	v_lshl_add_u64 v[0:1], v[132:133], 2, v[0:1]
	s_mov_b64 s[6:7], 0
	s_mov_b64 s[8:9], 0x1000
	s_movk_i32 s12, 0x1dff
	v_readlane_b32 s13, v253, 2
	v_readlane_b32 s16, v253, 5
	v_readlane_b32 s17, v253, 6
	v_readlane_b32 s18, v253, 7
	v_readlane_b32 s19, v253, 8
	v_readlane_b32 s20, v253, 9
	v_readlane_b32 s21, v253, 10
	v_readlane_b32 s22, v253, 11
	v_readlane_b32 s23, v253, 12
	v_readlane_b32 s24, v253, 13
	v_readlane_b32 s25, v253, 14
	v_readlane_b32 s26, v253, 15
	v_readlane_b32 s27, v253, 16
.LBB0_96:
	global_load_dword v174, v[0:1], off
	global_load_dword v175, v[0:1], off offset:2048
	v_lshl_add_u64 v[0:1], v[0:1], 0, s[8:9]
	global_load_dword v176, v[0:1], off
	global_load_dword v177, v[0:1], off offset:2048
	v_lshl_add_u64 v[0:1], v[0:1], 0, s[8:9]
	global_load_dword v178, v[0:1], off
	global_load_dword v179, v[0:1], off offset:2048
	v_lshl_add_u64 v[0:1], v[0:1], 0, s[8:9]
	global_load_dword v180, v[0:1], off
	global_load_dword v181, v[0:1], off offset:2048
	v_lshl_add_u64 v[0:1], v[0:1], 0, s[8:9]
	global_load_dword v182, v[0:1], off
	global_load_dword v183, v[0:1], off offset:2048
	v_lshl_add_u64 v[0:1], v[0:1], 0, s[8:9]
	global_load_dword v184, v[0:1], off
	global_load_dword v185, v[0:1], off offset:2048
	v_lshl_add_u64 v[0:1], v[0:1], 0, s[8:9]
	global_load_dword v186, v[0:1], off
	global_load_dword v187, v[0:1], off offset:2048
	v_lshl_add_u64 v[0:1], v[0:1], 0, s[8:9]
	global_load_dword v188, v[0:1], off
	global_load_dword v189, v[0:1], off offset:2048
	s_waitcnt vmcnt(15)
	v_mul_f32_e32 v5, 0xbfb8aa3b, v174
	v_exp_f32_e32 v5, v5
	s_nop 0
	v_add_f32_e32 v5, 1.0, v5
	v_rcp_f32_e32 v5, v5
	s_nop 0
	v_mul_f32_e32 v4, v174, v5
	ds_write_b32 v3, v4
	s_waitcnt vmcnt(14)
	v_mul_f32_e32 v5, 0xbfb8aa3b, v175
	v_exp_f32_e32 v5, v5
	s_nop 0
	v_add_f32_e32 v5, 1.0, v5
	v_rcp_f32_e32 v5, v5
	s_nop 0
	v_mul_f32_e32 v4, v175, v5
	ds_write_b32 v3, v4 offset:2048
	s_waitcnt vmcnt(13)
	v_mul_f32_e32 v5, 0xbfb8aa3b, v176
	v_exp_f32_e32 v5, v5
	s_nop 0
	v_add_f32_e32 v5, 1.0, v5
	v_rcp_f32_e32 v5, v5
	s_nop 0
	v_mul_f32_e32 v4, v176, v5
	ds_write_b32 v3, v4 offset:4096
	s_waitcnt vmcnt(12)
	v_mul_f32_e32 v5, 0xbfb8aa3b, v177
	v_exp_f32_e32 v5, v5
	s_nop 0
	v_add_f32_e32 v5, 1.0, v5
	v_rcp_f32_e32 v5, v5
	s_nop 0
	v_mul_f32_e32 v4, v177, v5
	ds_write_b32 v3, v4 offset:6144
	s_waitcnt vmcnt(11)
	v_mul_f32_e32 v5, 0xbfb8aa3b, v178
	v_exp_f32_e32 v5, v5
	s_nop 0
	v_add_f32_e32 v5, 1.0, v5
	v_rcp_f32_e32 v5, v5
	s_nop 0
	v_mul_f32_e32 v4, v178, v5
	ds_write_b32 v3, v4 offset:8192
	s_waitcnt vmcnt(10)
	v_mul_f32_e32 v5, 0xbfb8aa3b, v179
	v_exp_f32_e32 v5, v5
	s_nop 0
	v_add_f32_e32 v5, 1.0, v5
	v_rcp_f32_e32 v5, v5
	s_nop 0
	v_mul_f32_e32 v4, v179, v5
	ds_write_b32 v3, v4 offset:10240
	s_waitcnt vmcnt(9)
	v_mul_f32_e32 v5, 0xbfb8aa3b, v180
	v_exp_f32_e32 v5, v5
	s_nop 0
	v_add_f32_e32 v5, 1.0, v5
	v_rcp_f32_e32 v5, v5
	s_nop 0
	v_mul_f32_e32 v4, v180, v5
	ds_write_b32 v3, v4 offset:12288
	s_waitcnt vmcnt(8)
	v_mul_f32_e32 v5, 0xbfb8aa3b, v181
	v_exp_f32_e32 v5, v5
	s_nop 0
	v_add_f32_e32 v5, 1.0, v5
	v_rcp_f32_e32 v5, v5
	s_nop 0
	v_mul_f32_e32 v4, v181, v5
	ds_write_b32 v3, v4 offset:14336
	s_waitcnt vmcnt(7)
	v_mul_f32_e32 v5, 0xbfb8aa3b, v182
	v_exp_f32_e32 v5, v5
	s_nop 0
	v_add_f32_e32 v5, 1.0, v5
	v_rcp_f32_e32 v5, v5
	s_nop 0
	v_mul_f32_e32 v4, v182, v5
	ds_write_b32 v3, v4 offset:16384
	s_waitcnt vmcnt(6)
	v_mul_f32_e32 v5, 0xbfb8aa3b, v183
	v_exp_f32_e32 v5, v5
	s_nop 0
	v_add_f32_e32 v5, 1.0, v5
	v_rcp_f32_e32 v5, v5
	s_nop 0
	v_mul_f32_e32 v4, v183, v5
	ds_write_b32 v3, v4 offset:18432
	s_waitcnt vmcnt(5)
	v_mul_f32_e32 v5, 0xbfb8aa3b, v184
	v_exp_f32_e32 v5, v5
	s_nop 0
	v_add_f32_e32 v5, 1.0, v5
	v_rcp_f32_e32 v5, v5
	s_nop 0
	v_mul_f32_e32 v4, v184, v5
	ds_write_b32 v3, v4 offset:20480
	s_waitcnt vmcnt(4)
	v_mul_f32_e32 v5, 0xbfb8aa3b, v185
	v_exp_f32_e32 v5, v5
	s_nop 0
	v_add_f32_e32 v5, 1.0, v5
	v_rcp_f32_e32 v5, v5
	s_nop 0
	v_mul_f32_e32 v4, v185, v5
	ds_write_b32 v3, v4 offset:22528
	s_waitcnt vmcnt(3)
	v_mul_f32_e32 v5, 0xbfb8aa3b, v186
	v_exp_f32_e32 v5, v5
	s_nop 0
	v_add_f32_e32 v5, 1.0, v5
	v_rcp_f32_e32 v5, v5
	s_nop 0
	v_mul_f32_e32 v4, v186, v5
	ds_write_b32 v3, v4 offset:24576
	s_waitcnt vmcnt(2)
	v_mul_f32_e32 v5, 0xbfb8aa3b, v187
	v_exp_f32_e32 v5, v5
	s_nop 0
	v_add_f32_e32 v5, 1.0, v5
	v_rcp_f32_e32 v5, v5
	s_nop 0
	v_mul_f32_e32 v4, v187, v5
	ds_write_b32 v3, v4 offset:26624
	s_waitcnt vmcnt(1)
	v_mul_f32_e32 v5, 0xbfb8aa3b, v188
	v_exp_f32_e32 v5, v5
	s_nop 0
	v_add_f32_e32 v5, 1.0, v5
	v_rcp_f32_e32 v5, v5
	s_nop 0
	v_mul_f32_e32 v4, v188, v5
	ds_write_b32 v3, v4 offset:28672
	s_waitcnt vmcnt(0)
	v_mul_f32_e32 v5, 0xbfb8aa3b, v189
	v_exp_f32_e32 v5, v5
	s_nop 0
	v_add_f32_e32 v5, 1.0, v5
	v_rcp_f32_e32 v5, v5
	s_nop 0
	v_mul_f32_e32 v4, v189, v5
	ds_write_b32 v3, v4 offset:30720

.LBB0_1303:
	v_readlane_b32 s0, v253, 37
	v_readlane_b32 s2, v253, 39
	v_readlane_b32 s1, v253, 38
	v_readlane_b32 s3, v253, 40
	s_cmp_lt_i32 s2, 12
	s_cselect_b64 s[0:1], -1, 0
	s_cmp_gt_i32 s3, 11
	s_cselect_b64 s[2:3], -1, 0
	s_and_b64 s[0:1], s[0:1], s[2:3]
	s_and_b64 vcc, exec, s[0:1]
	s_cbranch_vccz .LBB0_1309
	s_mov_b32 s0, -1
	s_mov_b32 s1, 0
	v_mbcnt_lo_u32_b32 v0, s0, 0
	v_mbcnt_hi_u32_b32 v0, s0, v0
	v_readlane_b32 s0, v253, 41
	v_readlane_b32 s2, v253, 0
	s_nop 0
	v_lshl_add_u32 v0, s0, 6, v0
	s_nop 0
	v_readlane_b32 s0, v253, 35
	v_readlane_b32 s1, v253, 36
	s_load_dword s1, s[0:1], 0xa0
	v_readfirstlane_b32 s0, v0
	s_waitcnt lgkmcnt(0)
	s_ashr_i32 s0, s0, 6
	s_lshl_b32 s2, s2, 3
	s_add_i32 s0, s2, s0
	v_readlane_b32 s2, v253, 33
	v_readlane_b32 s3, v253, 34
	s_cmpk_gt_i32 s0, 0x3fff
	v_writelane_b32 v253, s2, 33
	s_nop 1
	v_writelane_b32 v253, s3, 34
	s_cbranch_scc1 .LBB0_1309
	v_readlane_b32 s2, v253, 33
	v_readlane_b32 s3, v253, 34
	s_add_u32 s8, s2, 0x19000000
	s_addc_u32 s9, s3, 0
	s_ashr_i32 s4, s0, 4
	s_ashr_i32 s5, s4, 31
	s_lshl_b32 s2, s1, 3
	s_lshl_b64 s[4:5], s[4:5], 16
	s_add_u32 s4, s8, s4
	s_addc_u32 s5, s9, s5
	v_lshlrev_b32_e32 v1, 3, v0
	s_lshl_b32 s3, s0, 5
	s_waitcnt vmcnt(0)
	v_and_b32_e32 v10, 0x1f8, v1
	v_and_b32_e32 v54, 24, v1
	s_and_b32 s3, s3, 0x1e0
	v_or_b32_e32 v1, s3, v54
	v_or_b32_e32 v11, 0x600, v10
	v_lshlrev_b32_e32 v32, 1, v1
	v_lshlrev_b32_e32 v1, 5, v11
	v_or_b32_e32 v12, 0x400, v10
	v_and_b32_e32 v34, 0xfc00, v1
	v_lshlrev_b32_e32 v1, 5, v12
	v_mov_b32_e32 v33, 0
	v_and_b32_e32 v36, 0xbc00, v1
	v_lshlrev_b32_e32 v1, 8, v0
	s_movk_i32 s3, 0x7c00
	v_mov_b32_e32 v6, 0x4000
	v_lshl_add_u64 v[2:3], s[4:5], 0, v[32:33]
	v_mov_b32_e32 v35, v33
	v_mov_b32_e32 v37, v33
	v_bitop3_b32 v38, v1, s3, v6 bitop3:0xc8
	v_mov_b32_e32 v39, v33
	v_and_b32_e32 v40, 0x3c00, v1
	v_mov_b32_e32 v41, v33
	v_lshl_add_u64 v[4:5], v[2:3], 0, v[34:35]
	v_lshl_add_u64 v[6:7], v[2:3], 0, v[38:39]
	v_lshl_add_u64 v[8:9], v[2:3], 0, v[40:41]
	v_lshl_add_u64 v[2:3], v[2:3], 0, v[36:37]
	global_load_dwordx4 v[24:27], v[6:7], off
	global_load_dwordx4 v[28:31], v[8:9], off
	global_load_dwordx4 v[16:19], v[2:3], off
	global_load_dwordx4 v[20:23], v[4:5], off
	v_readlane_b32 s12, v253, 17
	v_readlane_b32 s16, v253, 21
	v_readlane_b32 s17, v253, 22
	v_readlane_b32 s18, v253, 23
	v_readlane_b32 s19, v253, 24
	v_readlane_b32 s24, v253, 29
	v_readlane_b32 s25, v253, 30
	v_readlane_b32 s26, v253, 31
	v_readlane_b32 s27, v253, 32
	s_mov_b64 s[16:17], s[24:25]
	s_add_i32 s3, s0, s2
	s_lshl_b32 s10, s1, 8
	s_ashr_i32 s1, s0, 31
	s_mov_b64 s[18:19], s[26:27]
	s_lshl_b32 s11, s3, 5
	s_lshl_b64 s[4:5], s[0:1], 13
	v_lshlrev_b32_e32 v32, 2, v10
	v_and_b32_e32 v6, 63, v0
	v_readlane_b32 s13, v253, 18
	s_add_u32 s12, s18, s4
	v_lshl_add_u64 v[46:47], s[16:17], 0, v[32:33]
	v_or_b32_e32 v2, 0x1010, v32
	v_or_b32_e32 v32, 0x1810, v32
	v_mov_b32_e32 v1, v33
	v_lshlrev_b32_e32 v0, 2, v12
	s_addc_u32 s13, s19, s5
	v_lshl_add_u64 v[50:51], s[16:17], 0, v[32:33]
	v_lshlrev_b32_e32 v32, 5, v6
	s_mov_b64 s[6:7], 0x1000
	v_mov_b32_e32 v3, v33
	v_mov_b32_e32 v5, v33
	v_lshlrev_b32_e32 v4, 2, v11
	v_lshl_add_u64 v[42:43], s[16:17], 0, v[0:1]
	v_lshl_add_u64 v[0:1], s[12:13], 0, v[32:33]
	v_lshl_add_u64 v[44:45], s[16:17], 0, v[4:5]
	s_ashr_i32 s3, s2, 31
	v_lshl_add_u64 v[48:49], s[16:17], 0, v[2:3]
	v_lshl_add_u64 v[52:53], v[0:1], 0, s[6:7]
	v_mov_b32_e32 v55, 0x358637bd
	s_lshl_b64 s[4:5], s[2:3], 13
	v_readlane_b32 s14, v253, 19
	v_readlane_b32 s15, v253, 20
	v_readlane_b32 s20, v253, 25
	v_readlane_b32 s21, v253, 26
	v_readlane_b32 s22, v253, 27
	v_readlane_b32 s23, v253, 28
	global_load_dwordx4 v[120:123], v[46:47], off
	global_load_dwordx4 v[124:127], v[46:47], off offset:16
	global_load_dwordx4 v[128:131], v[46:47], off offset:2048
	global_load_dwordx4 v[132:135], v[46:47], off offset:2064
	global_load_dwordx4 v[136:139], v[42:43], off
	global_load_dwordx4 v[140:143], v[48:49], off
	global_load_dwordx4 v[144:147], v[44:45], off
	global_load_dwordx4 v[148:151], v[50:51], off
	s_waitcnt vmcnt(0)
	v_mov_b64_e32 v[4:5], v[24:25]
	s_waitcnt vmcnt(2)
	v_mov_b64_e32 v[0:1], v[28:29]
	s_waitcnt vmcnt(1)
	v_mov_b64_e32 v[8:9], v[16:17]
	s_waitcnt vmcnt(0)
	v_mov_b64_e32 v[12:13], v[20:21]
	v_mov_b64_e32 v[2:3], v[30:31]
	v_mov_b64_e32 v[6:7], v[26:27]
	v_mov_b64_e32 v[10:11], v[18:19]
	v_mov_b64_e32 v[14:15], v[22:23]
	s_branch .LBB0_1307
.LBB0_1306:
	v_cvt_f32_f16_sdwa v57, v28 dst_sel:DWORD dst_unused:UNUSED_PAD src0_sel:WORD_1
	v_cvt_f32_f16_e32 v56, v28
	v_cvt_f32_f16_sdwa v59, v29 dst_sel:DWORD dst_unused:UNUSED_PAD src0_sel:WORD_1
	v_cvt_f32_f16_e32 v58, v29
	v_cvt_f32_f16_sdwa v29, v30 dst_sel:DWORD dst_unused:UNUSED_PAD src0_sel:WORD_1
	v_cvt_f32_f16_e32 v28, v30
	v_cvt_f32_f16_sdwa v61, v31 dst_sel:DWORD dst_unused:UNUSED_PAD src0_sel:WORD_1
	v_cvt_f32_f16_e32 v60, v31
	v_cvt_f32_f16_sdwa v31, v24 dst_sel:DWORD dst_unused:UNUSED_PAD src0_sel:WORD_1
	v_cvt_f32_f16_e32 v30, v24
	v_cvt_f32_f16_sdwa v63, v25 dst_sel:DWORD dst_unused:UNUSED_PAD src0_sel:WORD_1
	v_cvt_f32_f16_e32 v62, v25
	v_cvt_f32_f16_sdwa v65, v26 dst_sel:DWORD dst_unused:UNUSED_PAD src0_sel:WORD_1
	v_cvt_f32_f16_e32 v64, v26
	v_cvt_f32_f16_sdwa v67, v27 dst_sel:DWORD dst_unused:UNUSED_PAD src0_sel:WORD_1
	v_cvt_f32_f16_e32 v66, v27
	v_cvt_f32_f16_sdwa v69, v16 dst_sel:DWORD dst_unused:UNUSED_PAD src0_sel:WORD_1
	v_cvt_f32_f16_e32 v68, v16
	v_cvt_f32_f16_sdwa v71, v17 dst_sel:DWORD dst_unused:UNUSED_PAD src0_sel:WORD_1
	v_cvt_f32_f16_e32 v70, v17
	v_cvt_f32_f16_sdwa v73, v18 dst_sel:DWORD dst_unused:UNUSED_PAD src0_sel:WORD_1
	v_cvt_f32_f16_e32 v72, v18
	v_cvt_f32_f16_sdwa v75, v19 dst_sel:DWORD dst_unused:UNUSED_PAD src0_sel:WORD_1
	v_cvt_f32_f16_e32 v74, v19
	v_cvt_f32_f16_sdwa v77, v20 dst_sel:DWORD dst_unused:UNUSED_PAD src0_sel:WORD_1
	v_cvt_f32_f16_e32 v76, v20
	v_cvt_f32_f16_sdwa v79, v21 dst_sel:DWORD dst_unused:UNUSED_PAD src0_sel:WORD_1
	v_cvt_f32_f16_e32 v78, v21
	v_cvt_f32_f16_sdwa v81, v22 dst_sel:DWORD dst_unused:UNUSED_PAD src0_sel:WORD_1
	v_cvt_f32_f16_e32 v80, v22
	v_cvt_f32_f16_sdwa v83, v23 dst_sel:DWORD dst_unused:UNUSED_PAD src0_sel:WORD_1
	v_cvt_f32_f16_e32 v82, v23
	v_pk_mul_f32 v[16:17], v[56:57], v[56:57]
	v_pk_mul_f32 v[18:19], v[58:59], v[58:59]
	v_pk_mul_f32 v[20:21], v[28:29], v[28:29]
	v_pk_mul_f32 v[22:23], v[60:61], v[60:61]
	v_pk_mul_f32 v[84:85], v[30:31], v[30:31]
	v_pk_mul_f32 v[86:87], v[62:63], v[62:63]
	v_add_f32_e32 v22, v22, v23
	v_add_f32_e32 v20, v20, v21
	v_add_f32_e32 v18, v18, v19
	v_add_f32_e32 v16, v16, v17
	v_add_f32_e32 v20, v20, v22
	v_add_f32_e32 v16, v16, v18
	v_add_f32_e32 v17, v86, v87
	v_add_f32_e32 v18, v84, v85
	v_pk_mul_f32 v[88:89], v[64:65], v[64:65]
	v_pk_mul_f32 v[90:91], v[66:67], v[66:67]
	v_add_f32_e32 v16, v16, v20
	v_add_f32_e32 v17, v18, v17
	v_add_f32_e32 v16, v16, v17
	v_add_f32_e32 v17, v90, v91
	v_add_f32_e32 v18, v88, v89
	v_pk_mul_f32 v[92:93], v[68:69], v[68:69]
	v_pk_mul_f32 v[94:95], v[70:71], v[70:71]
	v_add_f32_e32 v17, v18, v17
	v_add_f32_e32 v16, v17, v16
	v_add_f32_e32 v17, v94, v95
	v_add_f32_e32 v18, v92, v93
	v_pk_mul_f32 v[96:97], v[72:73], v[72:73]
	v_pk_mul_f32 v[98:99], v[74:75], v[74:75]
	v_add_f32_e32 v17, v18, v17
	v_add_f32_e32 v16, v17, v16
	v_add_f32_e32 v17, v98, v99
	v_add_f32_e32 v18, v96, v97
	v_pk_mul_f32 v[100:101], v[76:77], v[76:77]
	v_pk_mul_f32 v[102:103], v[78:79], v[78:79]
	v_add_f32_e32 v17, v18, v17
	v_add_f32_e32 v16, v17, v16
	v_add_f32_e32 v17, v102, v103
	v_add_f32_e32 v18, v100, v101
	v_pk_mul_f32 v[104:105], v[80:81], v[80:81]
	v_pk_mul_f32 v[106:107], v[82:83], v[82:83]
	v_add_f32_e32 v17, v18, v17
	v_add_f32_e32 v16, v17, v16
	v_add_f32_e32 v17, v106, v107
	v_add_f32_e32 v18, v104, v105
	v_add_f32_e32 v17, v18, v17
	v_add_f32_e32 v16, v17, v16
	s_add_i32 s11, s11, s10
	s_andn2_b64 vcc, exec, s[6:7]
	v_add_f32_dpp v16, v16, v16 row_ror:8 row_mask:0xf bank_mask:0xf bound_ctrl:1
	s_nop 1
	v_add_f32_dpp v16, v16, v16 row_ror:4 row_mask:0xf bank_mask:0xf bound_ctrl:1
	s_nop 1
	v_add_f32_dpp v16, v16, v16 row_ror:2 row_mask:0xf bank_mask:0xf bound_ctrl:1
	s_nop 1
	v_add_f32_dpp v16, v16, v16 row_ror:1 row_mask:0xf bank_mask:0xf bound_ctrl:1
	ds_swizzle_b32 v17, v16 offset:swizzle(SWAP,16)
	s_waitcnt lgkmcnt(0)
	v_add_f32_e32 v16, v16, v17
	s_nop 0
	v_readlane_b32 s3, v16, 32
	v_readlane_b32 s1, v16, 0
	s_nop 0
	v_mov_b32_e32 v16, s3
	v_add_f32_e32 v16, s1, v16
	v_fmamk_f32 v16, v16, 0x3a000000, v55
	v_rsq_f32_e32 v32, v16
	s_nop 0
	v_pk_mul_f32 v[16:17], v[56:57], v[32:33] op_sel_hi:[1,0]
	v_pk_mul_f32 v[18:19], v[58:59], v[32:33] op_sel_hi:[1,0]
	v_pk_mul_f32 v[20:21], v[60:61], v[32:33] op_sel_hi:[1,0]
	v_pk_mul_f32 v[22:23], v[28:29], v[32:33] op_sel_hi:[1,0]
	v_pk_mul_f32 v[16:17], v[120:121], v[16:17]
	v_pk_mul_f32 v[18:19], v[122:123], v[18:19]
	global_store_dwordx4 v[52:53], v[16:19], off offset:-4096
	v_pk_mul_f32 v[56:57], v[82:83], v[32:33] op_sel_hi:[1,0]
	v_pk_mul_f32 v[58:59], v[80:81], v[32:33] op_sel_hi:[1,0]
	v_pk_mul_f32 v[16:17], v[124:125], v[22:23]
	v_pk_mul_f32 v[18:19], v[126:127], v[20:21]
	global_store_dwordx4 v[52:53], v[16:19], off offset:-4080
	v_pk_mul_f32 v[20:21], v[62:63], v[32:33] op_sel_hi:[1,0]
	v_pk_mul_f32 v[22:23], v[30:31], v[32:33] op_sel_hi:[1,0]
	v_pk_mul_f32 v[16:17], v[128:129], v[22:23]
	v_pk_mul_f32 v[18:19], v[130:131], v[20:21]
	global_store_dwordx4 v[52:53], v[16:19], off offset:-2048
	v_pk_mul_f32 v[20:21], v[66:67], v[32:33] op_sel_hi:[1,0]
	v_pk_mul_f32 v[22:23], v[64:65], v[32:33] op_sel_hi:[1,0]
	v_pk_mul_f32 v[18:19], v[134:135], v[20:21]
	v_pk_mul_f32 v[16:17], v[132:133], v[22:23]
	global_store_dwordx4 v[52:53], v[16:19], off offset:-2032
	v_pk_mul_f32 v[20:21], v[70:71], v[32:33] op_sel_hi:[1,0]
	v_pk_mul_f32 v[22:23], v[68:69], v[32:33] op_sel_hi:[1,0]
	v_pk_mul_f32 v[18:19], v[20:21], v[138:139]
	v_pk_mul_f32 v[16:17], v[22:23], v[136:137]
	global_store_dwordx4 v[52:53], v[16:19], off
	v_pk_mul_f32 v[20:21], v[74:75], v[32:33] op_sel_hi:[1,0]
	v_pk_mul_f32 v[22:23], v[72:73], v[32:33] op_sel_hi:[1,0]
	v_pk_mul_f32 v[18:19], v[20:21], v[142:143]
	v_pk_mul_f32 v[16:17], v[22:23], v[140:141]
	global_store_dwordx4 v[52:53], v[16:19], off offset:16
	v_pk_mul_f32 v[20:21], v[78:79], v[32:33] op_sel_hi:[1,0]
	v_pk_mul_f32 v[22:23], v[76:77], v[32:33] op_sel_hi:[1,0]
	v_pk_mul_f32 v[18:19], v[20:21], v[146:147]
	v_pk_mul_f32 v[16:17], v[22:23], v[144:145]
	global_store_dwordx4 v[52:53], v[16:19], off offset:2048
	v_pk_mul_f32 v[20:21], v[58:59], v[148:149]
	v_pk_mul_f32 v[22:23], v[56:57], v[150:151]
	s_nop 0
	global_store_dwordx4 v[52:53], v[20:23], off offset:2064
	v_lshl_add_u64 v[52:53], v[52:53], 0, s[4:5]
	s_waitcnt vmcnt(8)
	v_mov_b64_e32 v[26:27], v[6:7]
	v_mov_b64_e32 v[24:25], v[4:5]
	v_mov_b64_e32 v[30:31], v[2:3]
	v_mov_b64_e32 v[28:29], v[0:1]
	v_mov_b64_e32 v[18:19], v[10:11]
	v_mov_b64_e32 v[16:17], v[8:9]
	v_mov_b64_e32 v[22:23], v[14:15]
	v_mov_b64_e32 v[20:21], v[12:13]
	s_cbranch_vccz .LBB0_1309
